# v31 + s_nop padding on in-place DPP broadcast pairs (hazard hygiene)
# speedup vs baseline: 1.0051x; 1.0013x over previous
.LBB4_56:
	s_waitcnt lgkmcnt(0)
	s_or_b64 exec, exec, s[6:7]
	s_nop 1
	v_add_u32_dpp v37, v36, v102 row_newbcast:0 row_mask:0xf bank_mask:0x3
	v_add_u32_dpp v37, v36, v102 row_newbcast:8 row_mask:0xf bank_mask:0xc
	v_add_u32_dpp v42, v36, v102 row_newbcast:1 row_mask:0xf bank_mask:0x3
	v_add_u32_dpp v42, v36, v102 row_newbcast:9 row_mask:0xf bank_mask:0xc
	ds_read_b128 v[38:41], v37 offset:52240
	ds_read_b128 v[42:45], v42 offset:52240
	v_add_u32_dpp v37, v36, v102 row_newbcast:2 row_mask:0xf bank_mask:0x3
	v_add_u32_dpp v37, v36, v102 row_newbcast:10 row_mask:0xf bank_mask:0xc
	v_add_u32_dpp v51, v36, v102 row_newbcast:3 row_mask:0xf bank_mask:0x3
	v_add_u32_dpp v51, v36, v102 row_newbcast:11 row_mask:0xf bank_mask:0xc
	v_mov_b32_dpp v60, v36 row_newbcast:5 row_mask:0xf bank_mask:0x3
	v_mov_b32_dpp v60, v36 row_newbcast:13 row_mask:0xf bank_mask:0xc
	ds_read_b128 v[46:49], v37 offset:52240
	ds_read_b128 v[56:59], v51 offset:52240
	v_add_u32_dpp v37, v36, v102 row_newbcast:4 row_mask:0xf bank_mask:0x3
	v_add_u32_dpp v37, v36, v102 row_newbcast:12 row_mask:0xf bank_mask:0xc
	v_mov_b32_dpp v50, v36 row_newbcast:6 row_mask:0xf bank_mask:0x3
	v_mov_b32_dpp v50, v36 row_newbcast:14 row_mask:0xf bank_mask:0xc
	v_mov_b32_dpp v36, v36 row_newbcast:7 row_mask:0xf bank_mask:0x3
	s_nop 1
	v_mov_b32_dpp v36, v36 row_newbcast:15 row_mask:0xf bank_mask:0xc
	v_add_u32_e32 v51, v102, v60
	ds_read_b128 v[60:63], v37 offset:52240
	ds_read_b128 v[64:67], v51 offset:52240
	s_add_i32 s22, s22, 8
	v_add_u32_e32 v37, v102, v50
	v_add_u32_e32 v36, v102, v36
	ds_read_b128 v[68:71], v37 offset:52240
	ds_read_b128 v[74:77], v36 offset:52240
	s_waitcnt lgkmcnt(7)
	v_pk_fma_f16 v36, v73, v38, v52
	v_pk_fma_f16 v37, v73, v39, v53
	v_pk_fma_f16 v38, v73, v40, v54
	v_pk_fma_f16 v39, v73, v41, v55
	s_waitcnt lgkmcnt(6)
	v_pk_fma_f16 v38, v73, v44, v38
	v_pk_fma_f16 v39, v73, v45, v39
	v_pk_fma_f16 v37, v73, v43, v37
	v_pk_fma_f16 v36, v73, v42, v36
	s_waitcnt lgkmcnt(5)
	v_pk_fma_f16 v37, v73, v47, v37
	v_pk_fma_f16 v36, v73, v46, v36
	v_pk_fma_f16 v38, v73, v48, v38
	v_pk_fma_f16 v39, v73, v49, v39
	s_waitcnt lgkmcnt(4)
	v_pk_fma_f16 v38, v73, v58, v38
	v_pk_fma_f16 v39, v73, v59, v39
	v_pk_fma_f16 v37, v73, v57, v37
	v_pk_fma_f16 v36, v73, v56, v36
	s_waitcnt lgkmcnt(3)
	v_pk_fma_f16 v37, v73, v61, v37
	v_pk_fma_f16 v36, v73, v60, v36
	v_pk_fma_f16 v38, v73, v62, v38
	v_pk_fma_f16 v39, v73, v63, v39
	s_waitcnt lgkmcnt(2)
	v_pk_fma_f16 v38, v73, v66, v38
	v_pk_fma_f16 v39, v73, v67, v39
	v_pk_fma_f16 v37, v73, v65, v37
	v_pk_fma_f16 v36, v73, v64, v36
	s_waitcnt lgkmcnt(1)
	v_pk_fma_f16 v37, v73, v69, v37
	v_pk_fma_f16 v36, v73, v68, v36
	v_pk_fma_f16 v38, v73, v70, v38
	v_pk_fma_f16 v39, v73, v71, v39
	s_waitcnt lgkmcnt(0)
	v_pk_fma_f16 v54, v73, v76, v38
	v_pk_fma_f16 v55, v73, v77, v39
	v_pk_fma_f16 v53, v73, v75, v37
	v_pk_fma_f16 v52, v73, v74, v36

.LBB4_75:
	s_waitcnt lgkmcnt(0)
	s_or_b64 exec, exec, s[6:7]
	s_nop 1
	v_add_u32_dpp v53, v52, v102 row_newbcast:0 row_mask:0xf bank_mask:0x3
	v_add_u32_dpp v53, v52, v102 row_newbcast:8 row_mask:0xf bank_mask:0xc
	v_add_u32_dpp v58, v52, v102 row_newbcast:1 row_mask:0xf bank_mask:0x3
	v_add_u32_dpp v58, v52, v102 row_newbcast:9 row_mask:0xf bank_mask:0xc
	ds_read_b128 v[54:57], v53 offset:52240
	ds_read_b128 v[58:61], v58 offset:52240
	v_add_u32_dpp v53, v52, v102 row_newbcast:2 row_mask:0xf bank_mask:0x3
	v_add_u32_dpp v53, v52, v102 row_newbcast:10 row_mask:0xf bank_mask:0xc
	v_add_u32_dpp v67, v52, v102 row_newbcast:3 row_mask:0xf bank_mask:0x3
	v_add_u32_dpp v67, v52, v102 row_newbcast:11 row_mask:0xf bank_mask:0xc
	v_mov_b32_dpp v76, v52 row_newbcast:5 row_mask:0xf bank_mask:0x3
	v_mov_b32_dpp v76, v52 row_newbcast:13 row_mask:0xf bank_mask:0xc
	ds_read_b128 v[62:65], v53 offset:52240
	ds_read_b128 v[72:75], v67 offset:52240
	v_add_u32_dpp v53, v52, v102 row_newbcast:4 row_mask:0xf bank_mask:0x3
	v_add_u32_dpp v53, v52, v102 row_newbcast:12 row_mask:0xf bank_mask:0xc
	v_mov_b32_dpp v66, v52 row_newbcast:6 row_mask:0xf bank_mask:0x3
	v_mov_b32_dpp v66, v52 row_newbcast:14 row_mask:0xf bank_mask:0xc
	v_mov_b32_dpp v52, v52 row_newbcast:7 row_mask:0xf bank_mask:0x3
	s_nop 1
	v_mov_b32_dpp v52, v52 row_newbcast:15 row_mask:0xf bank_mask:0xc
	v_add_u32_e32 v67, v102, v76
	ds_read_b128 v[76:79], v53 offset:52240
	ds_read_b128 v[80:83], v67 offset:52240
	s_add_i32 s22, s22, 8
	v_add_u32_e32 v53, v102, v66
	v_add_u32_e32 v52, v102, v52
	ds_read_b128 v[84:87], v53 offset:52240
	ds_read_b128 v[110:113], v52 offset:52240
	s_waitcnt lgkmcnt(7)
	v_pk_fma_f16 v52, v32, v54, v68
	v_pk_fma_f16 v53, v32, v55, v69
	v_pk_fma_f16 v54, v32, v56, v70
	v_pk_fma_f16 v55, v32, v57, v71
	s_waitcnt lgkmcnt(6)
	v_pk_fma_f16 v54, v32, v60, v54
	v_pk_fma_f16 v55, v32, v61, v55
	v_pk_fma_f16 v53, v32, v59, v53
	v_pk_fma_f16 v52, v32, v58, v52
	s_waitcnt lgkmcnt(5)
	v_pk_fma_f16 v53, v32, v63, v53
	v_pk_fma_f16 v52, v32, v62, v52
	v_pk_fma_f16 v54, v32, v64, v54
	v_pk_fma_f16 v55, v32, v65, v55
	s_waitcnt lgkmcnt(4)
	v_pk_fma_f16 v54, v32, v74, v54
	v_pk_fma_f16 v55, v32, v75, v55
	v_pk_fma_f16 v53, v32, v73, v53
	v_pk_fma_f16 v52, v32, v72, v52
	s_waitcnt lgkmcnt(3)
	v_pk_fma_f16 v53, v32, v77, v53
	v_pk_fma_f16 v52, v32, v76, v52
	v_pk_fma_f16 v54, v32, v78, v54
	v_pk_fma_f16 v55, v32, v79, v55
	s_waitcnt lgkmcnt(2)
	v_pk_fma_f16 v54, v32, v82, v54
	v_pk_fma_f16 v55, v32, v83, v55
	v_pk_fma_f16 v53, v32, v81, v53
	v_pk_fma_f16 v52, v32, v80, v52
	s_waitcnt lgkmcnt(1)
	v_pk_fma_f16 v53, v32, v85, v53
	v_pk_fma_f16 v52, v32, v84, v52
	v_pk_fma_f16 v54, v32, v86, v54
	v_pk_fma_f16 v55, v32, v87, v55
	s_waitcnt lgkmcnt(0)
	v_pk_fma_f16 v70, v32, v112, v54
	v_pk_fma_f16 v71, v32, v113, v55
	v_pk_fma_f16 v69, v32, v111, v53
	v_pk_fma_f16 v68, v32, v110, v52

.LBB4_94:
	s_waitcnt lgkmcnt(0)
	s_or_b64 exec, exec, s[6:7]
	s_nop 1
	v_mov_b32_dpp v52, v34 row_newbcast:0 row_mask:0xf bank_mask:0x3
	v_mov_b32_dpp v52, v34 row_newbcast:8 row_mask:0xf bank_mask:0xc
	v_mov_b32_dpp v53, v34 row_newbcast:1 row_mask:0xf bank_mask:0x3
	v_mov_b32_dpp v53, v34 row_newbcast:9 row_mask:0xf bank_mask:0xc
	v_mov_b32_dpp v60, v34 row_newbcast:2 row_mask:0xf bank_mask:0x3
	v_mov_b32_dpp v60, v34 row_newbcast:10 row_mask:0xf bank_mask:0xc
	v_mov_b32_dpp v61, v34 row_newbcast:3 row_mask:0xf bank_mask:0x3
	v_mov_b32_dpp v61, v34 row_newbcast:11 row_mask:0xf bank_mask:0xc
	v_mov_b32_dpp v72, v34 row_newbcast:4 row_mask:0xf bank_mask:0x3
	v_mov_b32_dpp v72, v34 row_newbcast:12 row_mask:0xf bank_mask:0xc
	v_mov_b32_dpp v73, v34 row_newbcast:5 row_mask:0xf bank_mask:0x3
	v_mov_b32_dpp v73, v34 row_newbcast:13 row_mask:0xf bank_mask:0xc
	v_mov_b32_dpp v80, v34 row_newbcast:6 row_mask:0xf bank_mask:0x3
	v_mov_b32_dpp v80, v34 row_newbcast:14 row_mask:0xf bank_mask:0xc
	v_mov_b32_dpp v34, v34 row_newbcast:7 row_mask:0xf bank_mask:0x3
	s_nop 1
	v_mov_b32_dpp v34, v34 row_newbcast:15 row_mask:0xf bank_mask:0xc
	v_add_u32_e32 v52, v102, v52
	v_add_u32_e32 v56, v102, v53
	ds_read_b128 v[52:55], v52 offset:52240
	ds_read_b128 v[56:59], v56 offset:52240
	v_add_u32_e32 v60, v102, v60
	v_add_u32_e32 v64, v102, v61
	ds_read_b128 v[60:63], v60 offset:52240
	ds_read_b128 v[64:67], v64 offset:52240
	v_add_u32_e32 v72, v102, v72
	v_add_u32_e32 v76, v102, v73
	v_add_u32_e32 v80, v102, v80
	v_add_u32_e32 v34, v102, v34
	ds_read_b128 v[72:75], v72 offset:52240
	ds_read_b128 v[76:79], v76 offset:52240
	ds_read_b128 v[80:83], v80 offset:52240
	ds_read_b128 v[84:87], v34 offset:52240
	s_waitcnt lgkmcnt(7)
	v_pk_fma_f16 v34, v32, v52, v68
	v_pk_fma_f16 v52, v32, v53, v69
	v_pk_fma_f16 v53, v32, v54, v70
	v_pk_fma_f16 v54, v32, v55, v71
	s_waitcnt lgkmcnt(6)
	v_pk_fma_f16 v53, v32, v58, v53
	v_pk_fma_f16 v54, v32, v59, v54
	v_pk_fma_f16 v52, v32, v57, v52
	v_pk_fma_f16 v34, v32, v56, v34
	s_waitcnt lgkmcnt(5)
	v_pk_fma_f16 v52, v32, v61, v52
	v_pk_fma_f16 v34, v32, v60, v34
	v_pk_fma_f16 v53, v32, v62, v53
	v_pk_fma_f16 v54, v32, v63, v54
	s_waitcnt lgkmcnt(4)
	v_pk_fma_f16 v53, v32, v66, v53
	v_pk_fma_f16 v54, v32, v67, v54
	v_pk_fma_f16 v52, v32, v65, v52
	v_pk_fma_f16 v34, v32, v64, v34
	s_waitcnt lgkmcnt(3)
	v_pk_fma_f16 v52, v32, v73, v52
	v_pk_fma_f16 v34, v32, v72, v34
	v_pk_fma_f16 v53, v32, v74, v53
	v_pk_fma_f16 v54, v32, v75, v54
	s_waitcnt lgkmcnt(2)
	v_pk_fma_f16 v53, v32, v78, v53
	v_pk_fma_f16 v54, v32, v79, v54
	v_pk_fma_f16 v52, v32, v77, v52
	v_pk_fma_f16 v34, v32, v76, v34
	s_waitcnt lgkmcnt(1)
	v_pk_fma_f16 v52, v32, v81, v52
	v_pk_fma_f16 v34, v32, v80, v34
	v_pk_fma_f16 v53, v32, v82, v53
	v_pk_fma_f16 v54, v32, v83, v54
	s_waitcnt lgkmcnt(0)
	v_pk_fma_f16 v70, v32, v86, v53
	v_pk_fma_f16 v71, v32, v87, v54
	v_pk_fma_f16 v69, v32, v85, v52
	v_pk_fma_f16 v68, v32, v84, v34
	s_add_i32 s22, s22, 8

.Lp2_after_idx:
	v_add_u32_e32 v102, s33, v77
	v_cmp_gt_i32_e32 vcc, s28, v102
	v_mov_b32_e32 v103, -1
	s_and_b64 s[8:9], s[2:3], vcc
	s_mov_b64 s[6:7], exec
	s_and_b64 exec, exec, s[8:9]
	v_lshlrev_b32_e32 v102, 2, v102
	global_load_dword v103, v102, s[16:17]
	s_mov_b64 exec, s[6:7]
	s_waitcnt vmcnt(0)
	v_lshlrev_b32_e32 v9, 6, v9
	v_lshlrev_b32_e32 v8, 6, v8
	v_lshlrev_b32_e32 v60, 6, v60
	v_lshlrev_b32_e32 v59, 6, v59
	v_lshlrev_b32_e32 v62, 6, v62
	v_lshlrev_b32_e32 v89, 6, v89
	v_lshlrev_b32_e32 v88, 6, v88
	v_lshlrev_b32_e32 v86, 6, v86
	v_lshlrev_b32_e32 v7, 6, v7
	v_and_b32_e32 v9, 0x7fffc0, v9
	v_and_b32_e32 v8, 0x7fffc0, v8
	v_and_b32_e32 v60, 0x7fffc0, v60
	v_and_b32_e32 v59, 0x7fffc0, v59
	v_and_b32_e32 v62, 0x7fffc0, v62
	v_and_b32_e32 v89, 0x7fffc0, v89
	v_and_b32_e32 v88, 0x7fffc0, v88
	v_and_b32_e32 v86, 0x7fffc0, v86
	v_and_b32_e32 v7, 0x7fffc0, v7
	v_mov_b32_dpp v12, v9 row_newbcast:2 row_mask:0xf bank_mask:0x3
	v_mov_b32_dpp v12, v9 row_newbcast:10 row_mask:0xf bank_mask:0xc
	v_mov_b32_dpp v14, v9 row_newbcast:4 row_mask:0xf bank_mask:0x3
	v_mov_b32_dpp v14, v9 row_newbcast:12 row_mask:0xf bank_mask:0xc
	v_mov_b32_dpp v15, v9 row_newbcast:5 row_mask:0xf bank_mask:0x3
	v_mov_b32_dpp v15, v9 row_newbcast:13 row_mask:0xf bank_mask:0xc
	v_add_u32_dpp v10, v9, v81 row_newbcast:0 row_mask:0xf bank_mask:0x3
	v_add_u32_dpp v10, v9, v81 row_newbcast:8 row_mask:0xf bank_mask:0xc
	v_add_u32_dpp v11, v9, v81 row_newbcast:1 row_mask:0xf bank_mask:0x3
	v_add_u32_dpp v11, v9, v81 row_newbcast:9 row_mask:0xf bank_mask:0xc
	v_add_u32_dpp v13, v9, v81 row_newbcast:3 row_mask:0xf bank_mask:0x3
	v_add_u32_dpp v13, v9, v81 row_newbcast:11 row_mask:0xf bank_mask:0xc
	v_mov_b32_dpp v16, v9 row_newbcast:6 row_mask:0xf bank_mask:0x3
	v_mov_b32_dpp v16, v9 row_newbcast:14 row_mask:0xf bank_mask:0xc
	v_mov_b32_dpp v9, v9 row_newbcast:7 row_mask:0xf bank_mask:0x3
	s_nop 1
	v_mov_b32_dpp v9, v9 row_newbcast:15 row_mask:0xf bank_mask:0xc
	v_add_u32_e32 v12, v12, v81
	global_load_dwordx2 v[56:57], v10, s[30:31]
	global_load_dwordx2 v[52:53], v11, s[30:31]
	global_load_dwordx2 v[30:31], v12, s[30:31]
	global_load_dwordx2 v[24:25], v13, s[30:31]
	v_add_u32_e32 v10, v14, v81
	v_add_u32_e32 v11, v15, v81
	v_add_u32_e32 v9, v9, v81
	v_add_u32_e32 v12, v16, v81
	v_mov_b32_dpp v16, v8 row_newbcast:3 row_mask:0xf bank_mask:0x3
	v_mov_b32_dpp v16, v8 row_newbcast:11 row_mask:0xf bank_mask:0xc
	global_load_dwordx2 v[54:55], v10, s[30:31]
	global_load_dwordx2 v[50:51], v11, s[30:31]
	global_load_dwordx2 v[26:27], v12, s[30:31]
	global_load_dwordx2 v[20:21], v9, s[30:31]
	v_add_u32_dpp v9, v8, v81 row_newbcast:0 row_mask:0xf bank_mask:0x3
	v_add_u32_dpp v9, v8, v81 row_newbcast:8 row_mask:0xf bank_mask:0xc
	v_add_u32_dpp v10, v8, v81 row_newbcast:1 row_mask:0xf bank_mask:0x3
	v_add_u32_dpp v10, v8, v81 row_newbcast:9 row_mask:0xf bank_mask:0xc
	v_add_u32_dpp v11, v8, v81 row_newbcast:2 row_mask:0xf bank_mask:0x3
	v_add_u32_dpp v11, v8, v81 row_newbcast:10 row_mask:0xf bank_mask:0xc
	v_mov_b32_dpp v13, v8 row_newbcast:4 row_mask:0xf bank_mask:0x3
	v_mov_b32_dpp v13, v8 row_newbcast:12 row_mask:0xf bank_mask:0xc
	v_mov_b32_dpp v14, v8 row_newbcast:5 row_mask:0xf bank_mask:0x3
	v_mov_b32_dpp v14, v8 row_newbcast:13 row_mask:0xf bank_mask:0xc
	v_mov_b32_dpp v15, v8 row_newbcast:6 row_mask:0xf bank_mask:0x3
	v_mov_b32_dpp v15, v8 row_newbcast:14 row_mask:0xf bank_mask:0xc
	v_mov_b32_dpp v8, v8 row_newbcast:7 row_mask:0xf bank_mask:0x3
	s_nop 1
	v_mov_b32_dpp v8, v8 row_newbcast:15 row_mask:0xf bank_mask:0xc
	v_add_u32_e32 v12, v16, v81
	global_load_dwordx2 v[28:29], v9, s[30:31]
	global_load_dwordx2 v[22:23], v10, s[30:31]
	global_load_dwordx2 v[18:19], v11, s[30:31]
	global_load_dwordx2 v[16:17], v12, s[30:31]
	v_add_u32_e32 v9, v13, v81
	v_add_u32_e32 v10, v14, v81
	v_add_u32_e32 v11, v15, v81
	v_add_u32_e32 v8, v8, v81
	global_load_dwordx2 v[14:15], v9, s[30:31]
	global_load_dwordx2 v[12:13], v10, s[30:31]
	s_nop 0
	global_load_dwordx2 v[10:11], v11, s[30:31]
	s_nop 0
	global_load_dwordx2 v[8:9], v8, s[30:31]
	v_cmp_lt_i32_e32 vcc, 16, v58
	s_cmp_lg_u64 vcc, 0
	s_cselect_b64 s[36:37], -1, 0
	v_cmp_lt_i32_e64 s[10:11], 18, v58
	v_cmp_lt_i32_e64 s[8:9], 20, v58
	v_cmp_lt_i32_e64 s[6:7], 22, v58
	s_cbranch_vccz .LBB5_42
	v_add_u32_dpp v34, v60, v81 row_newbcast:0 row_mask:0xf bank_mask:0x3
	v_add_u32_dpp v34, v60, v81 row_newbcast:8 row_mask:0xf bank_mask:0xc
	v_add_u32_dpp v38, v60, v81 row_newbcast:1 row_mask:0xf bank_mask:0x3
	v_add_u32_dpp v38, v60, v81 row_newbcast:9 row_mask:0xf bank_mask:0xc
	global_load_dwordx2 v[34:35], v34, s[30:31]
	s_nop 0
	global_load_dwordx2 v[38:39], v38, s[30:31]

.LBB5_90:
	s_cmp_lg_u64 s[6:7], 0
	s_cselect_b64 s[8:9], -1, 0
	s_cmp_eq_u64 s[6:7], 0
	s_cbranch_scc1 .LBB5_92
	v_mov_b32_dpp v44, v7 row_newbcast:6 row_mask:0xf bank_mask:0x3
	v_mov_b32_dpp v44, v7 row_newbcast:14 row_mask:0xf bank_mask:0xc
	v_mov_b32_dpp v7, v7 row_newbcast:7 row_mask:0xf bank_mask:0x3
	s_nop 1
	v_mov_b32_dpp v7, v7 row_newbcast:15 row_mask:0xf bank_mask:0xc
	v_add_u32_e32 v44, v44, v81
	v_add_u32_e32 v7, v7, v81
	global_load_dwordx2 v[44:45], v44, s[30:31]
	s_nop 0
	global_load_dwordx2 v[48:49], v7, s[30:31]
